# S5 Toeplitz-tap (KT) loop: scalar loads pull the next BBAR block into L2 one block ahead
# baseline (speedup 1.0000x reference)
; __device__ __forceinline__ void ph1_small(const Args& a, int tid, int wave, int lane, int G, int bid) {
;     ...
; #pragma unroll 8
;             for (int n = 0; n < 64; ++n) { const float cr = cre[((size_t)g * 16 + p) * 64 + n], ci = cim[((size_t)g * 16 + p) * 64 + n];
;                 const float pr = POW[(((size_t)g * 65 + tau) * 64 + n) * 2], pi = POW[(((size_t)g * 65 + tau) * 64 + n) * 2 + 1];
;                 const float er = cr * pr - ci * pi, ei = cr * pi + ci * pr;
;                 const f32x4* bp = (const f32x4*)(BBAR + ((size_t)g * 64 + n) * 32);
; #pragma unroll
;                 for (int q = 0; q < 8; ++q) { const f32x4 bb = bp[q]; s[2 * q] += er * bb[0] - ei * bb[1]; s[2 * q + 1] += er * bb[2] - ei * bb[3]; } }
.LBB0_108:
	s_waitcnt lgkmcnt(0)
	v_lshl_add_u64 v[6:7], v[44:45], 0, s[48:49]
	global_load_dwordx4 v[2:5], v[6:7], off offset:16
	global_load_dwordx4 v[18:21], v[6:7], off
	v_lshl_add_u64 v[6:7], v[42:43], 0, s[48:49]
	global_load_dwordx4 v[10:13], v[6:7], off offset:16
	global_load_dwordx4 v[22:25], v[6:7], off
	v_lshl_add_u64 v[6:7], s[74:75], 0, v[40:41]
	s_mov_b64 s[70:71], 0x600000
	s_mov_b32 s33, 0x600000
	v_lshl_add_u64 v[26:27], v[6:7], 0, s[70:71]
	v_add_co_u32_e32 v6, vcc, s33, v6
	v_lshl_add_u64 v[48:49], s[74:75], 0, v[38:39]
	s_nop 0
	v_addc_co_u32_e32 v7, vcc, 0, v7, vcc
	global_load_dwordx4 v[70:73], v[6:7], off
	s_nop 0
	global_load_dwordx4 v[6:9], v[26:27], off offset:48
	global_load_dwordx4 v[14:17], v[26:27], off offset:32
	s_nop 0
	global_load_dwordx4 v[26:29], v[26:27], off offset:16
	s_mov_b32 s33, 0x500000
	s_mov_b64 s[70:71], 0x500000
	v_lshl_add_u64 v[86:87], v[48:49], 0, s[70:71]
	s_mov_b64 s[70:71], 0x500040
	v_readfirstlane_b32 s98, v48
	v_readfirstlane_b32 s99, v49
	s_add_u32 s98, s98, 0x500400
	s_addc_u32 s99, s99, 0
	s_nop 0
	s_load_dword s100, s[98:99], 0x0
	s_load_dword s101, s[98:99], 0x80
	s_load_dword s100, s[98:99], 0x100
	s_load_dword s101, s[98:99], 0x180
	s_load_dword s100, s[98:99], 0x200
	s_load_dword s101, s[98:99], 0x280
	s_load_dword s100, s[98:99], 0x300
	s_load_dword s101, s[98:99], 0x380
	s_add_u32 s48, s48, 32
	s_addc_u32 s49, s49, 0
	v_lshl_add_u64 v[40:41], v[40:41], 0, 64
	s_cmpk_eq_i32 s48, 0x100
	s_waitcnt vmcnt(6)
	v_mov_b32_e32 v46, v18
	s_waitcnt vmcnt(4)
	v_mov_b32_e32 v47, v22
	s_waitcnt vmcnt(3)
	v_pk_mul_f32 v[66:67], v[46:47], v[70:71]
	v_mov_b32_e32 v46, v22
	v_mov_b32_e32 v47, v18
	v_pk_mul_f32 v[70:71], v[46:47], v[70:71]
	v_add_co_u32_e32 v46, vcc, s33, v48
	v_pk_add_f32 v[70:71], v[70:71], v[70:71] op_sel:[0,1] op_sel_hi:[0,1]
	s_nop 0
	v_addc_co_u32_e32 v47, vcc, 0, v49, vcc
	global_load_dwordx4 v[74:77], v[46:47], off
	global_load_dwordx4 v[78:81], v[86:87], off offset:48
	global_load_dwordx4 v[82:85], v[86:87], off offset:32
	s_nop 0
	global_load_dwordx4 v[86:89], v[86:87], off offset:16
	v_pk_add_f32 v[66:67], v[66:67], v[66:67] op_sel:[0,1] op_sel_hi:[0,1] neg_lo:[0,1] neg_hi:[0,1]
	v_mov_b32_e32 v22, v19
	v_mov_b32_e32 v18, v23
	v_pk_mul_f32 v[18:19], v[18:19], v[72:73]
	s_waitcnt vmcnt(3)
	v_mov_b32_e32 v91, v76
	v_mov_b32_e32 v76, v75
	v_mov_b32_e32 v90, v74
	v_pk_mul_f32 v[74:75], v[70:71], v[76:77]
	v_pk_add_f32 v[18:19], v[18:19], v[18:19] op_sel:[0,1] op_sel_hi:[0,1]
	v_pk_fma_f32 v[74:75], v[66:67], v[90:91], v[74:75] neg_lo:[0,0,1] neg_hi:[0,0,1]
	s_nop 0
	v_pk_add_f32 v[90:91], v[56:57], v[74:75]
	s_waitcnt vmcnt(0)
	v_mov_b32_e32 v57, v88
	v_mov_b32_e32 v88, v87
	v_mov_b32_e32 v56, v86
	v_pk_mul_f32 v[74:75], v[70:71], v[88:89]
	s_nop 0
	v_pk_fma_f32 v[56:57], v[66:67], v[56:57], v[74:75] neg_lo:[0,0,1] neg_hi:[0,0,1]
	s_nop 0
	v_pk_add_f32 v[86:87], v[54:55], v[56:57]
	v_mov_b32_e32 v55, v84
	v_mov_b32_e32 v84, v83
	v_mov_b32_e32 v54, v82
	v_pk_mul_f32 v[56:57], v[70:71], v[84:85]
	s_nop 0
	v_pk_fma_f32 v[54:55], v[66:67], v[54:55], v[56:57] neg_lo:[0,0,1] neg_hi:[0,0,1]
	s_nop 0
	v_pk_add_f32 v[82:83], v[52:53], v[54:55]
	v_mov_b32_e32 v53, v80
	v_mov_b32_e32 v80, v79
	v_mov_b32_e32 v52, v78
	v_pk_mul_f32 v[54:55], v[70:71], v[80:81]
	v_lshl_add_u64 v[78:79], v[48:49], 0, s[70:71]
	v_pk_fma_f32 v[52:53], v[66:67], v[52:53], v[54:55] neg_lo:[0,0,1] neg_hi:[0,0,1]
	s_mov_b64 s[70:71], 0x500080
	v_pk_add_f32 v[84:85], v[50:51], v[52:53]
	global_load_dwordx4 v[50:53], v[46:47], off offset:64
	global_load_dwordx4 v[54:57], v[78:79], off offset:48
	global_load_dwordx4 v[74:77], v[78:79], off offset:32
	s_nop 0
	global_load_dwordx4 v[78:81], v[78:79], off offset:16
	s_waitcnt vmcnt(3)
	v_mov_b32_e32 v89, v52
	v_mov_b32_e32 v52, v51
	v_mov_b32_e32 v88, v50
	v_pk_mul_f32 v[50:51], v[70:71], v[52:53]
	s_nop 0
	v_pk_fma_f32 v[50:51], v[66:67], v[88:89], v[50:51] neg_lo:[0,0,1] neg_hi:[0,0,1]
	s_nop 0
	v_pk_add_f32 v[88:89], v[58:59], v[50:51]
	s_waitcnt vmcnt(0)
	v_mov_b32_e32 v51, v80
	v_mov_b32_e32 v80, v79
	v_mov_b32_e32 v50, v78
	v_pk_mul_f32 v[52:53], v[70:71], v[80:81]
	s_nop 0
	v_pk_fma_f32 v[50:51], v[66:67], v[50:51], v[52:53] neg_lo:[0,0,1] neg_hi:[0,0,1]
	s_nop 0
	v_pk_add_f32 v[78:79], v[60:61], v[50:51]
	v_mov_b32_e32 v51, v76
	v_mov_b32_e32 v76, v75
	v_mov_b32_e32 v50, v74
	v_pk_mul_f32 v[52:53], v[70:71], v[76:77]
	s_nop 0
	v_pk_fma_f32 v[50:51], v[66:67], v[50:51], v[52:53] neg_lo:[0,0,1] neg_hi:[0,0,1]
	s_nop 0
	v_pk_add_f32 v[74:75], v[64:65], v[50:51]
	v_mov_b32_e32 v51, v56
	v_mov_b32_e32 v56, v55
	v_mov_b32_e32 v50, v54
	v_pk_mul_f32 v[52:53], v[70:71], v[56:57]
	v_pk_mul_f32 v[70:71], v[22:23], v[72:73]
	v_pk_fma_f32 v[50:51], v[66:67], v[50:51], v[52:53] neg_lo:[0,0,1] neg_hi:[0,0,1]
	v_lshl_add_u64 v[22:23], v[48:49], 0, s[70:71]
	v_pk_add_f32 v[66:67], v[62:63], v[50:51]
	global_load_dwordx4 v[50:53], v[46:47], off offset:128
	global_load_dwordx4 v[54:57], v[22:23], off offset:48
	global_load_dwordx4 v[58:61], v[22:23], off offset:32
	global_load_dwordx4 v[62:65], v[22:23], off offset:16
	v_pk_add_f32 v[22:23], v[70:71], v[70:71] op_sel:[0,1] op_sel_hi:[0,1] neg_lo:[0,1] neg_hi:[0,1]
	s_mov_b64 s[70:71], 0x5000c0
	s_waitcnt vmcnt(3)
	v_mov_b32_e32 v71, v52
	v_mov_b32_e32 v52, v51
	v_mov_b32_e32 v70, v50
	v_pk_mul_f32 v[50:51], v[18:19], v[52:53]
	s_nop 0
	v_pk_fma_f32 v[50:51], v[22:23], v[70:71], v[50:51] neg_lo:[0,0,1] neg_hi:[0,0,1]
	s_nop 0
	v_pk_add_f32 v[90:91], v[90:91], v[50:51]
	s_waitcnt vmcnt(0)
; __device__ __forceinline__ void ph1_small(const Args& a, int tid, int wave, int lane, int G, int bid) {
;     ...
;             for (int n = 0; n < 64; ++n) { const float cr = cre[((size_t)g * 16 + p) * 64 + n], ci = cim[((size_t)g * 16 + p) * 64 + n];
;                 const float pr = POW[(((size_t)g * 65 + tau) * 64 + n) * 2], pi = POW[(((size_t)g * 65 + tau) * 64 + n) * 2 + 1];
;                 const float er = cr * pr - ci * pi, ei = cr * pi + ci * pr;
;                 const f32x4* bp = (const f32x4*)(BBAR + ((size_t)g * 64 + n) * 32);
; #pragma unroll
;                 for (int q = 0; q < 8; ++q) { const f32x4 bb = bp[q]; s[2 * q] += er * bb[0] - ei * bb[1]; s[2 * q + 1] += er * bb[2] - ei * bb[3]; } }
	v_mov_b32_e32 v51, v64
	v_mov_b32_e32 v64, v63
	v_mov_b32_e32 v50, v62
	v_pk_mul_f32 v[52:53], v[18:19], v[64:65]
	s_nop 0
	v_pk_fma_f32 v[50:51], v[22:23], v[50:51], v[52:53] neg_lo:[0,0,1] neg_hi:[0,0,1]
	s_nop 0
	v_pk_add_f32 v[86:87], v[86:87], v[50:51]
	v_mov_b32_e32 v51, v60
	v_mov_b32_e32 v60, v59
	v_mov_b32_e32 v50, v58
	v_pk_mul_f32 v[52:53], v[18:19], v[60:61]
	s_nop 0
	v_pk_fma_f32 v[50:51], v[22:23], v[50:51], v[52:53] neg_lo:[0,0,1] neg_hi:[0,0,1]
	s_nop 0
	v_pk_add_f32 v[82:83], v[82:83], v[50:51]
	v_mov_b32_e32 v51, v56
	v_mov_b32_e32 v56, v55
	v_mov_b32_e32 v50, v54
	v_pk_mul_f32 v[52:53], v[18:19], v[56:57]
	v_lshl_add_u64 v[54:55], v[48:49], 0, s[70:71]
	v_pk_fma_f32 v[50:51], v[22:23], v[50:51], v[52:53] neg_lo:[0,0,1] neg_hi:[0,0,1]
	s_mov_b64 s[70:71], 0x500100
	v_pk_add_f32 v[84:85], v[84:85], v[50:51]
	global_load_dwordx4 v[50:53], v[46:47], off offset:192
	global_load_dwordx4 v[58:61], v[54:55], off offset:48
	global_load_dwordx4 v[62:65], v[54:55], off offset:32
	s_nop 0
	global_load_dwordx4 v[54:57], v[54:55], off offset:16
	s_waitcnt vmcnt(3)
	v_mov_b32_e32 v71, v52
	v_mov_b32_e32 v52, v51
	v_mov_b32_e32 v70, v50
	v_pk_mul_f32 v[50:51], v[18:19], v[52:53]
	s_nop 0
	v_pk_fma_f32 v[50:51], v[22:23], v[70:71], v[50:51] neg_lo:[0,0,1] neg_hi:[0,0,1]
	s_nop 0
	v_pk_add_f32 v[52:53], v[88:89], v[50:51]
	s_waitcnt vmcnt(0)
	v_mov_b32_e32 v51, v56
	v_mov_b32_e32 v56, v55
	v_mov_b32_e32 v50, v54
	v_pk_mul_f32 v[54:55], v[18:19], v[56:57]
	s_nop 0
	v_pk_fma_f32 v[50:51], v[22:23], v[50:51], v[54:55] neg_lo:[0,0,1] neg_hi:[0,0,1]
	s_nop 0
	v_pk_add_f32 v[54:55], v[78:79], v[50:51]
	v_mov_b32_e32 v51, v64
	v_mov_b32_e32 v64, v63
	v_mov_b32_e32 v50, v62
	v_pk_mul_f32 v[56:57], v[18:19], v[64:65]
	s_nop 0
	v_pk_fma_f32 v[50:51], v[22:23], v[50:51], v[56:57] neg_lo:[0,0,1] neg_hi:[0,0,1]
	s_nop 0
	v_pk_add_f32 v[56:57], v[74:75], v[50:51]
	v_mov_b32_e32 v51, v60
	v_mov_b32_e32 v60, v59
	v_mov_b32_e32 v50, v58
	v_pk_mul_f32 v[18:19], v[18:19], v[60:61]
	s_nop 0
	v_pk_fma_f32 v[18:19], v[22:23], v[50:51], v[18:19] neg_lo:[0,0,1] neg_hi:[0,0,1]
	v_mov_b32_e32 v22, v24
	v_pk_add_f32 v[58:59], v[66:67], v[18:19]
	v_mov_b32_e32 v18, v20
	v_mov_b32_e32 v19, v24
	v_mov_b32_e32 v23, v20
	v_pk_mul_f32 v[18:19], v[18:19], v[26:27]
	v_pk_mul_f32 v[22:23], v[22:23], v[26:27]
	v_lshl_add_u64 v[26:27], v[48:49], 0, s[70:71]
	global_load_dwordx4 v[64:67], v[46:47], off offset:256
	global_load_dwordx4 v[70:73], v[26:27], off offset:48
	global_load_dwordx4 v[74:77], v[26:27], off offset:32
	global_load_dwordx4 v[78:81], v[26:27], off offset:16
	v_pk_add_f32 v[60:61], v[18:19], v[18:19] op_sel:[0,1] op_sel_hi:[0,1] neg_lo:[0,1] neg_hi:[0,1]
	v_pk_add_f32 v[62:63], v[22:23], v[22:23] op_sel:[0,1] op_sel_hi:[0,1]
	s_mov_b64 s[70:71], 0x500140
	v_mov_b32_e32 v24, v21
	v_mov_b32_e32 v20, v25
	v_pk_mul_f32 v[20:21], v[20:21], v[28:29]
	s_waitcnt vmcnt(3)
	v_mov_b32_e32 v19, v66
	v_mov_b32_e32 v66, v65
	v_mov_b32_e32 v18, v64
	v_pk_mul_f32 v[22:23], v[62:63], v[66:67]
	s_nop 0
	v_pk_fma_f32 v[18:19], v[60:61], v[18:19], v[22:23] neg_lo:[0,0,1] neg_hi:[0,0,1]
	s_waitcnt vmcnt(0)
	v_mov_b32_e32 v23, v80
	v_mov_b32_e32 v80, v79
	v_mov_b32_e32 v22, v78
	v_pk_mul_f32 v[26:27], v[62:63], v[80:81]
	v_lshl_add_u64 v[78:79], v[48:49], 0, s[70:71]
	v_pk_fma_f32 v[22:23], v[60:61], v[22:23], v[26:27] neg_lo:[0,0,1] neg_hi:[0,0,1]
	v_mov_b32_e32 v27, v76
	v_mov_b32_e32 v76, v75
	v_mov_b32_e32 v26, v74
	v_pk_mul_f32 v[50:51], v[62:63], v[76:77]
	s_mov_b64 s[70:71], 0x500180
	v_pk_fma_f32 v[26:27], v[60:61], v[26:27], v[50:51] neg_lo:[0,0,1] neg_hi:[0,0,1]
	v_mov_b32_e32 v51, v72
	v_mov_b32_e32 v72, v71
	v_mov_b32_e32 v50, v70
	v_pk_mul_f32 v[64:65], v[62:63], v[72:73]
	v_pk_add_f32 v[26:27], v[82:83], v[26:27]
	v_pk_fma_f32 v[50:51], v[60:61], v[50:51], v[64:65] neg_lo:[0,0,1] neg_hi:[0,0,1]
	global_load_dwordx4 v[64:67], v[46:47], off offset:320
	global_load_dwordx4 v[70:73], v[78:79], off offset:48
	global_load_dwordx4 v[74:77], v[78:79], off offset:32
	s_nop 0
	global_load_dwordx4 v[78:81], v[78:79], off offset:16
	v_pk_add_f32 v[18:19], v[90:91], v[18:19]
	v_pk_add_f32 v[22:23], v[86:87], v[22:23]
	v_pk_add_f32 v[50:51], v[84:85], v[50:51]
	s_waitcnt vmcnt(3)
	v_mov_b32_e32 v83, v66
	v_mov_b32_e32 v66, v65
	v_mov_b32_e32 v82, v64
	v_pk_mul_f32 v[64:65], v[62:63], v[66:67]
	s_nop 0
	v_pk_fma_f32 v[64:65], v[60:61], v[82:83], v[64:65] neg_lo:[0,0,1] neg_hi:[0,0,1]
	s_nop 0
	v_pk_add_f32 v[64:65], v[52:53], v[64:65]
	s_waitcnt vmcnt(0)
	v_mov_b32_e32 v53, v80
	v_mov_b32_e32 v80, v79
	v_mov_b32_e32 v52, v78
	v_pk_mul_f32 v[66:67], v[62:63], v[80:81]
	v_pk_mul_f32 v[78:79], v[24:25], v[28:29]
	v_pk_fma_f32 v[52:53], v[60:61], v[52:53], v[66:67] neg_lo:[0,0,1] neg_hi:[0,0,1]
	v_lshl_add_u64 v[24:25], v[48:49], 0, s[70:71]
	v_pk_add_f32 v[66:67], v[54:55], v[52:53]
	v_mov_b32_e32 v53, v76
	v_mov_b32_e32 v76, v75
	v_mov_b32_e32 v52, v74
	v_pk_mul_f32 v[54:55], v[62:63], v[76:77]
	v_pk_add_f32 v[80:81], v[20:21], v[20:21] op_sel:[0,1] op_sel_hi:[0,1]
	v_pk_fma_f32 v[52:53], v[60:61], v[52:53], v[54:55] neg_lo:[0,0,1] neg_hi:[0,0,1]
	v_pk_add_f32 v[78:79], v[78:79], v[78:79] op_sel:[0,1] op_sel_hi:[0,1] neg_lo:[0,1] neg_hi:[0,1]
	v_pk_add_f32 v[56:57], v[56:57], v[52:53]
	v_mov_b32_e32 v53, v72
	v_mov_b32_e32 v72, v71
	v_mov_b32_e32 v52, v70
	v_pk_mul_f32 v[54:55], v[62:63], v[72:73]
	s_mov_b64 s[70:71], 0x5001c0
	v_pk_fma_f32 v[52:53], v[60:61], v[52:53], v[54:55] neg_lo:[0,0,1] neg_hi:[0,0,1]
	s_nop 0
	v_pk_add_f32 v[58:59], v[58:59], v[52:53]
	global_load_dwordx4 v[52:55], v[46:47], off offset:384
	global_load_dwordx4 v[60:63], v[24:25], off offset:48
	global_load_dwordx4 v[70:73], v[24:25], off offset:32
	global_load_dwordx4 v[74:77], v[24:25], off offset:16
	s_waitcnt vmcnt(3)
; __device__ __forceinline__ void ph1_small(const Args& a, int tid, int wave, int lane, int G, int bid) {
;     ...
;             for (int n = 0; n < 64; ++n) { const float cr = cre[((size_t)g * 16 + p) * 64 + n], ci = cim[((size_t)g * 16 + p) * 64 + n];
;                 const float pr = POW[(((size_t)g * 65 + tau) * 64 + n) * 2], pi = POW[(((size_t)g * 65 + tau) * 64 + n) * 2 + 1];
;                 const float er = cr * pr - ci * pi, ei = cr * pi + ci * pr;
;                 const f32x4* bp = (const f32x4*)(BBAR + ((size_t)g * 64 + n) * 32);
; #pragma unroll
;                 for (int q = 0; q < 8; ++q) { const f32x4 bb = bp[q]; s[2 * q] += er * bb[0] - ei * bb[1]; s[2 * q + 1] += er * bb[2] - ei * bb[3]; } }
	v_mov_b32_e32 v25, v54
	v_mov_b32_e32 v54, v53
	v_mov_b32_e32 v24, v52
	v_pk_mul_f32 v[20:21], v[80:81], v[54:55]
	s_nop 0
	v_pk_fma_f32 v[20:21], v[78:79], v[24:25], v[20:21] neg_lo:[0,0,1] neg_hi:[0,0,1]
	s_nop 0
	v_pk_add_f32 v[28:29], v[18:19], v[20:21]
	s_waitcnt vmcnt(0)
	v_mov_b32_e32 v19, v76
	v_mov_b32_e32 v76, v75
	v_mov_b32_e32 v18, v74
	v_pk_mul_f32 v[20:21], v[80:81], v[76:77]
	s_nop 0
	v_pk_fma_f32 v[18:19], v[78:79], v[18:19], v[20:21] neg_lo:[0,0,1] neg_hi:[0,0,1]
	s_nop 0
	v_pk_add_f32 v[52:53], v[22:23], v[18:19]
	v_mov_b32_e32 v19, v72
	v_mov_b32_e32 v72, v71
	v_mov_b32_e32 v18, v70
	v_pk_mul_f32 v[20:21], v[80:81], v[72:73]
	v_lshl_add_u64 v[22:23], v[48:49], 0, s[70:71]
	v_pk_fma_f32 v[18:19], v[78:79], v[18:19], v[20:21] neg_lo:[0,0,1] neg_hi:[0,0,1]
	s_mov_b64 s[70:71], 0x500200
	v_pk_add_f32 v[54:55], v[26:27], v[18:19]
	v_mov_b32_e32 v19, v62
	v_mov_b32_e32 v62, v61
	v_mov_b32_e32 v18, v60
	v_pk_mul_f32 v[20:21], v[80:81], v[62:63]
	s_nop 0
	v_pk_fma_f32 v[18:19], v[78:79], v[18:19], v[20:21] neg_lo:[0,0,1] neg_hi:[0,0,1]
	s_nop 0
	v_pk_add_f32 v[50:51], v[50:51], v[18:19]
	global_load_dwordx4 v[18:21], v[46:47], off offset:448
	global_load_dwordx4 v[24:27], v[22:23], off offset:48
	global_load_dwordx4 v[60:63], v[22:23], off offset:32
	global_load_dwordx4 v[70:73], v[22:23], off offset:16
	s_waitcnt vmcnt(3)
	v_mov_b32_e32 v23, v20
	v_mov_b32_e32 v20, v19
	v_mov_b32_e32 v22, v18
	v_pk_mul_f32 v[18:19], v[80:81], v[20:21]
	s_waitcnt vmcnt(0)
	v_mov_b32_e32 v21, v72
	v_mov_b32_e32 v72, v71
	v_pk_fma_f32 v[18:19], v[78:79], v[22:23], v[18:19] neg_lo:[0,0,1] neg_hi:[0,0,1]
	v_mov_b32_e32 v20, v70
	v_pk_mul_f32 v[22:23], v[80:81], v[72:73]
	v_lshl_add_u64 v[70:71], v[48:49], 0, s[70:71]
	v_pk_fma_f32 v[20:21], v[78:79], v[20:21], v[22:23] neg_lo:[0,0,1] neg_hi:[0,0,1]
	v_mov_b32_e32 v23, v62
	v_mov_b32_e32 v62, v61
	v_mov_b32_e32 v22, v60
	v_pk_mul_f32 v[60:61], v[80:81], v[62:63]
	v_pk_add_f32 v[18:19], v[64:65], v[18:19]
	v_pk_fma_f32 v[22:23], v[78:79], v[22:23], v[60:61] neg_lo:[0,0,1] neg_hi:[0,0,1]
	v_pk_add_f32 v[20:21], v[66:67], v[20:21]
	v_pk_add_f32 v[22:23], v[56:57], v[22:23]
	v_mov_b32_e32 v57, v26
	v_mov_b32_e32 v26, v25
	v_mov_b32_e32 v56, v24
	v_pk_mul_f32 v[24:25], v[80:81], v[26:27]
	v_mov_b32_e32 v26, v2
	v_pk_fma_f32 v[24:25], v[78:79], v[56:57], v[24:25] neg_lo:[0,0,1] neg_hi:[0,0,1]
	v_mov_b32_e32 v27, v10
	v_mov_b32_e32 v56, v10
	v_mov_b32_e32 v57, v2
	v_pk_add_f32 v[24:25], v[58:59], v[24:25]
	v_pk_mul_f32 v[26:27], v[26:27], v[14:15]
	v_pk_mul_f32 v[14:15], v[56:57], v[14:15]
	global_load_dwordx4 v[56:59], v[46:47], off offset:512
	global_load_dwordx4 v[60:63], v[70:71], off offset:48
	global_load_dwordx4 v[64:67], v[70:71], off offset:32
	s_nop 0
	global_load_dwordx4 v[70:73], v[70:71], off offset:16
	v_pk_add_f32 v[74:75], v[26:27], v[26:27] op_sel:[0,1] op_sel_hi:[0,1] neg_lo:[0,1] neg_hi:[0,1]
	v_pk_add_f32 v[76:77], v[14:15], v[14:15] op_sel:[0,1] op_sel_hi:[0,1]
	s_mov_b64 s[70:71], 0x500240
	v_mov_b32_e32 v10, v3
	v_mov_b32_e32 v2, v11
	v_pk_mul_f32 v[2:3], v[2:3], v[16:17]
	s_waitcnt vmcnt(3)
	v_mov_b32_e32 v27, v58
	v_mov_b32_e32 v58, v57
	v_mov_b32_e32 v26, v56
	v_pk_mul_f32 v[14:15], v[76:77], v[58:59]
	s_nop 0
	v_pk_fma_f32 v[14:15], v[74:75], v[26:27], v[14:15] neg_lo:[0,0,1] neg_hi:[0,0,1]
	s_waitcnt vmcnt(0)
	v_mov_b32_e32 v27, v72
	v_mov_b32_e32 v72, v71
	v_pk_add_f32 v[14:15], v[28:29], v[14:15]
	v_mov_b32_e32 v26, v70
	v_pk_mul_f32 v[28:29], v[76:77], v[72:73]
	s_nop 0
	v_pk_fma_f32 v[26:27], v[74:75], v[26:27], v[28:29] neg_lo:[0,0,1] neg_hi:[0,0,1]
	v_mov_b32_e32 v29, v66
	v_mov_b32_e32 v66, v65
	v_pk_add_f32 v[26:27], v[52:53], v[26:27]
	v_mov_b32_e32 v28, v64
	v_pk_mul_f32 v[52:53], v[76:77], v[66:67]
	v_lshl_add_u64 v[64:65], v[48:49], 0, s[70:71]
	v_pk_fma_f32 v[28:29], v[74:75], v[28:29], v[52:53] neg_lo:[0,0,1] neg_hi:[0,0,1]
	v_mov_b32_e32 v53, v62
	v_mov_b32_e32 v62, v61
	v_pk_add_f32 v[28:29], v[54:55], v[28:29]
	v_mov_b32_e32 v52, v60
	v_pk_mul_f32 v[54:55], v[76:77], v[62:63]
	s_mov_b64 s[70:71], 0x500280
	v_pk_fma_f32 v[52:53], v[74:75], v[52:53], v[54:55] neg_lo:[0,0,1] neg_hi:[0,0,1]
	s_nop 0
	v_pk_add_f32 v[50:51], v[50:51], v[52:53]
	global_load_dwordx4 v[52:55], v[46:47], off offset:576
	global_load_dwordx4 v[56:59], v[64:65], off offset:48
	global_load_dwordx4 v[60:63], v[64:65], off offset:32
	s_nop 0
	global_load_dwordx4 v[64:67], v[64:65], off offset:16
	s_waitcnt vmcnt(3)
	v_mov_b32_e32 v71, v54
	v_mov_b32_e32 v54, v53
	v_mov_b32_e32 v70, v52
	v_pk_mul_f32 v[52:53], v[76:77], v[54:55]
	s_nop 0
	v_pk_fma_f32 v[52:53], v[74:75], v[70:71], v[52:53] neg_lo:[0,0,1] neg_hi:[0,0,1]
	s_nop 0
	v_pk_add_f32 v[18:19], v[18:19], v[52:53]
	s_waitcnt vmcnt(0)
	v_mov_b32_e32 v53, v66
	v_mov_b32_e32 v66, v65
	v_mov_b32_e32 v52, v64
	v_pk_mul_f32 v[54:55], v[76:77], v[66:67]
	s_nop 0
	v_pk_fma_f32 v[52:53], v[74:75], v[52:53], v[54:55] neg_lo:[0,0,1] neg_hi:[0,0,1]
	s_nop 0
	v_pk_add_f32 v[20:21], v[20:21], v[52:53]
	v_mov_b32_e32 v53, v62
	v_mov_b32_e32 v62, v61
	v_mov_b32_e32 v52, v60
	v_pk_mul_f32 v[54:55], v[76:77], v[62:63]
	s_nop 0
	v_pk_fma_f32 v[52:53], v[74:75], v[52:53], v[54:55] neg_lo:[0,0,1] neg_hi:[0,0,1]
	s_nop 0
	v_pk_add_f32 v[22:23], v[22:23], v[52:53]
	v_mov_b32_e32 v53, v58
	v_mov_b32_e32 v58, v57
	v_mov_b32_e32 v52, v56
	v_pk_mul_f32 v[54:55], v[76:77], v[58:59]
	s_nop 0
	v_pk_fma_f32 v[52:53], v[74:75], v[52:53], v[54:55] neg_lo:[0,0,1] neg_hi:[0,0,1]
	v_pk_add_f32 v[54:55], v[2:3], v[2:3] op_sel:[0,1] op_sel_hi:[0,1]
	v_pk_add_f32 v[24:25], v[24:25], v[52:53]
	v_pk_mul_f32 v[52:53], v[10:11], v[16:17]
	v_lshl_add_u64 v[10:11], v[48:49], 0, s[70:71]
	global_load_dwordx4 v[56:59], v[46:47], off offset:640
	global_load_dwordx4 v[60:63], v[10:11], off offset:48
	global_load_dwordx4 v[64:67], v[10:11], off offset:32
	global_load_dwordx4 v[70:73], v[10:11], off offset:16
	v_pk_add_f32 v[52:53], v[52:53], v[52:53] op_sel:[0,1] op_sel_hi:[0,1] neg_lo:[0,1] neg_hi:[0,1]
	s_mov_b64 s[70:71], 0x5002c0
	s_waitcnt vmcnt(3)
; __device__ __forceinline__ void ph1_small(const Args& a, int tid, int wave, int lane, int G, int bid) {
;     ...
;             for (int n = 0; n < 64; ++n) { const float cr = cre[((size_t)g * 16 + p) * 64 + n], ci = cim[((size_t)g * 16 + p) * 64 + n];
;                 const float pr = POW[(((size_t)g * 65 + tau) * 64 + n) * 2], pi = POW[(((size_t)g * 65 + tau) * 64 + n) * 2 + 1];
;                 const float er = cr * pr - ci * pi, ei = cr * pi + ci * pr;
;                 const f32x4* bp = (const f32x4*)(BBAR + ((size_t)g * 64 + n) * 32);
; #pragma unroll
;                 for (int q = 0; q < 8; ++q) { const f32x4 bb = bp[q]; s[2 * q] += er * bb[0] - ei * bb[1]; s[2 * q + 1] += er * bb[2] - ei * bb[3]; } }
	v_mov_b32_e32 v11, v58
	v_mov_b32_e32 v58, v57
	v_mov_b32_e32 v10, v56
	v_pk_mul_f32 v[2:3], v[54:55], v[58:59]
	s_nop 0
	v_pk_fma_f32 v[2:3], v[52:53], v[10:11], v[2:3] neg_lo:[0,0,1] neg_hi:[0,0,1]
	s_waitcnt vmcnt(0)
	v_mov_b32_e32 v11, v72
	v_mov_b32_e32 v72, v71
	v_pk_add_f32 v[2:3], v[14:15], v[2:3]
	v_mov_b32_e32 v10, v70
	v_pk_mul_f32 v[14:15], v[54:55], v[72:73]
	s_nop 0
	v_pk_fma_f32 v[10:11], v[52:53], v[10:11], v[14:15] neg_lo:[0,0,1] neg_hi:[0,0,1]
	v_mov_b32_e32 v15, v66
	v_mov_b32_e32 v66, v65
	v_mov_b32_e32 v14, v64
	v_pk_mul_f32 v[16:17], v[54:55], v[66:67]
	v_pk_add_f32 v[10:11], v[26:27], v[10:11]
	v_pk_fma_f32 v[14:15], v[52:53], v[14:15], v[16:17] neg_lo:[0,0,1] neg_hi:[0,0,1]
	v_mov_b32_e32 v17, v62
	v_mov_b32_e32 v62, v61
	v_mov_b32_e32 v16, v60
	v_pk_mul_f32 v[26:27], v[54:55], v[62:63]
	v_pk_add_f32 v[14:15], v[28:29], v[14:15]
	v_pk_fma_f32 v[16:17], v[52:53], v[16:17], v[26:27] neg_lo:[0,0,1] neg_hi:[0,0,1]
	s_nop 0
	v_pk_add_f32 v[16:17], v[50:51], v[16:17]
	v_lshl_add_u64 v[50:51], v[48:49], 0, s[70:71]
	global_load_dwordx4 v[26:29], v[46:47], off offset:704
	global_load_dwordx4 v[56:59], v[50:51], off offset:48
	global_load_dwordx4 v[60:63], v[50:51], off offset:32
	global_load_dwordx4 v[64:67], v[50:51], off offset:16
	s_mov_b64 s[70:71], 0x500300
	s_waitcnt vmcnt(3)
	v_mov_b32_e32 v51, v28
	v_mov_b32_e32 v28, v27
	v_mov_b32_e32 v50, v26
	v_pk_mul_f32 v[26:27], v[54:55], v[28:29]
	s_nop 0
	v_pk_fma_f32 v[26:27], v[52:53], v[50:51], v[26:27] neg_lo:[0,0,1] neg_hi:[0,0,1]
	s_nop 0
	v_pk_add_f32 v[18:19], v[18:19], v[26:27]
	s_waitcnt vmcnt(0)
	v_mov_b32_e32 v27, v66
	v_mov_b32_e32 v66, v65
	v_mov_b32_e32 v26, v64
	v_pk_mul_f32 v[28:29], v[54:55], v[66:67]
	s_nop 0
	v_pk_fma_f32 v[26:27], v[52:53], v[26:27], v[28:29] neg_lo:[0,0,1] neg_hi:[0,0,1]
	s_nop 0
	v_pk_add_f32 v[20:21], v[20:21], v[26:27]
	v_mov_b32_e32 v27, v62
	v_mov_b32_e32 v62, v61
	v_mov_b32_e32 v26, v60
	v_pk_mul_f32 v[28:29], v[54:55], v[62:63]
	s_nop 0
	v_pk_fma_f32 v[26:27], v[52:53], v[26:27], v[28:29] neg_lo:[0,0,1] neg_hi:[0,0,1]
	s_nop 0
	v_pk_add_f32 v[26:27], v[22:23], v[26:27]
	v_mov_b32_e32 v23, v58
	v_mov_b32_e32 v58, v57
	v_mov_b32_e32 v22, v56
	v_pk_mul_f32 v[28:29], v[54:55], v[58:59]
	s_nop 0
	v_pk_fma_f32 v[22:23], v[52:53], v[22:23], v[28:29] neg_lo:[0,0,1] neg_hi:[0,0,1]
	s_nop 0
	v_pk_add_f32 v[28:29], v[24:25], v[22:23]
	v_mov_b32_e32 v22, v4
	v_mov_b32_e32 v23, v12
	v_mov_b32_e32 v24, v12
	v_mov_b32_e32 v25, v4
	v_pk_mul_f32 v[22:23], v[22:23], v[6:7]
	v_pk_mul_f32 v[6:7], v[24:25], v[6:7]
	v_lshl_add_u64 v[24:25], v[48:49], 0, s[70:71]
	global_load_dwordx4 v[50:53], v[46:47], off offset:768
	global_load_dwordx4 v[54:57], v[24:25], off offset:48
	global_load_dwordx4 v[58:61], v[24:25], off offset:32
	global_load_dwordx4 v[62:65], v[24:25], off offset:16
	v_pk_add_f32 v[66:67], v[22:23], v[22:23] op_sel:[0,1] op_sel_hi:[0,1] neg_lo:[0,1] neg_hi:[0,1]
	v_pk_add_f32 v[70:71], v[6:7], v[6:7] op_sel:[0,1] op_sel_hi:[0,1]
	s_mov_b64 s[70:71], 0x500340
	v_mov_b32_e32 v12, v5
	v_mov_b32_e32 v4, v13
	v_pk_mul_f32 v[4:5], v[4:5], v[8:9]
	s_waitcnt vmcnt(3)
	v_mov_b32_e32 v23, v52
	v_mov_b32_e32 v52, v51
	v_mov_b32_e32 v22, v50
	v_pk_mul_f32 v[6:7], v[70:71], v[52:53]
	s_nop 0
	v_pk_fma_f32 v[6:7], v[66:67], v[22:23], v[6:7] neg_lo:[0,0,1] neg_hi:[0,0,1]
	s_nop 0
	v_pk_add_f32 v[2:3], v[2:3], v[6:7]
	s_waitcnt vmcnt(0)
	v_mov_b32_e32 v7, v64
	v_mov_b32_e32 v64, v63
	v_mov_b32_e32 v6, v62
	v_pk_mul_f32 v[22:23], v[70:71], v[64:65]
	s_nop 0
	v_pk_fma_f32 v[6:7], v[66:67], v[6:7], v[22:23] neg_lo:[0,0,1] neg_hi:[0,0,1]
	s_nop 0
	v_pk_add_f32 v[6:7], v[10:11], v[6:7]
	v_mov_b32_e32 v11, v60
	v_mov_b32_e32 v60, v59
	v_mov_b32_e32 v10, v58
	v_pk_mul_f32 v[22:23], v[70:71], v[60:61]
	s_nop 0
	v_pk_fma_f32 v[10:11], v[66:67], v[10:11], v[22:23] neg_lo:[0,0,1] neg_hi:[0,0,1]
	s_nop 0
	v_pk_add_f32 v[10:11], v[14:15], v[10:11]
	v_mov_b32_e32 v15, v56
	v_mov_b32_e32 v56, v55
	v_mov_b32_e32 v14, v54
	v_pk_mul_f32 v[22:23], v[70:71], v[56:57]
	s_nop 0
	v_pk_fma_f32 v[14:15], v[66:67], v[14:15], v[22:23] neg_lo:[0,0,1] neg_hi:[0,0,1]
	s_nop 0
	v_pk_add_f32 v[14:15], v[16:17], v[14:15]
	v_lshl_add_u64 v[16:17], v[48:49], 0, s[70:71]
	global_load_dwordx4 v[22:25], v[46:47], off offset:832
	global_load_dwordx4 v[50:53], v[16:17], off offset:48
	global_load_dwordx4 v[54:57], v[16:17], off offset:32
	global_load_dwordx4 v[58:61], v[16:17], off offset:16
	s_mov_b64 s[70:71], 0x500380
	s_waitcnt vmcnt(3)
	v_mov_b32_e32 v17, v24
	v_mov_b32_e32 v24, v23
	v_mov_b32_e32 v16, v22
	v_pk_mul_f32 v[22:23], v[70:71], v[24:25]
	s_nop 0
	v_pk_fma_f32 v[16:17], v[66:67], v[16:17], v[22:23] neg_lo:[0,0,1] neg_hi:[0,0,1]
	s_nop 0
	v_pk_add_f32 v[24:25], v[18:19], v[16:17]
	s_waitcnt vmcnt(0)
; __device__ __forceinline__ void ph1_small(const Args& a, int tid, int wave, int lane, int G, int bid) {
;     ...
;             for (int n = 0; n < 64; ++n) { const float cr = cre[((size_t)g * 16 + p) * 64 + n], ci = cim[((size_t)g * 16 + p) * 64 + n];
;                 const float pr = POW[(((size_t)g * 65 + tau) * 64 + n) * 2], pi = POW[(((size_t)g * 65 + tau) * 64 + n) * 2 + 1];
;                 const float er = cr * pr - ci * pi, ei = cr * pi + ci * pr;
;                 const f32x4* bp = (const f32x4*)(BBAR + ((size_t)g * 64 + n) * 32);
; #pragma unroll
;                 for (int q = 0; q < 8; ++q) { const f32x4 bb = bp[q]; s[2 * q] += er * bb[0] - ei * bb[1]; s[2 * q + 1] += er * bb[2] - ei * bb[3]; } }
;             { const float dv = (tau == 0) ? a.in[I_SD][g * 16 + p] : 0.0f;
; #pragma unroll
;               for (int q = 0; q < 16; ++q) s[q] += (q == p) ? dv : 0.0f; }
	v_mov_b32_e32 v17, v60
	v_mov_b32_e32 v60, v59
	v_mov_b32_e32 v16, v58
	v_pk_mul_f32 v[18:19], v[70:71], v[60:61]
	s_nop 0
	v_pk_fma_f32 v[16:17], v[66:67], v[16:17], v[18:19] neg_lo:[0,0,1] neg_hi:[0,0,1]
	s_nop 0
	v_pk_add_f32 v[22:23], v[20:21], v[16:17]
	v_mov_b32_e32 v17, v56
	v_mov_b32_e32 v56, v55
	v_mov_b32_e32 v16, v54
	v_pk_mul_f32 v[18:19], v[70:71], v[56:57]
	s_nop 0
	v_pk_fma_f32 v[16:17], v[66:67], v[16:17], v[18:19] neg_lo:[0,0,1] neg_hi:[0,0,1]
	s_nop 0
	v_pk_add_f32 v[20:21], v[26:27], v[16:17]
	v_mov_b32_e32 v17, v52
	v_mov_b32_e32 v52, v51
	v_mov_b32_e32 v16, v50
	v_pk_mul_f32 v[18:19], v[70:71], v[52:53]
	s_nop 0
	v_pk_fma_f32 v[16:17], v[66:67], v[16:17], v[18:19] neg_lo:[0,0,1] neg_hi:[0,0,1]
	s_nop 0
	v_pk_add_f32 v[18:19], v[28:29], v[16:17]
	v_pk_mul_f32 v[16:17], v[12:13], v[8:9]
	v_lshl_add_u64 v[8:9], v[48:49], 0, s[70:71]
	global_load_dwordx4 v[50:53], v[46:47], off offset:896
	global_load_dwordx4 v[58:61], v[8:9], off offset:48
	global_load_dwordx4 v[62:65], v[8:9], off offset:32
	global_load_dwordx4 v[70:73], v[8:9], off offset:16
	v_pk_add_f32 v[28:29], v[4:5], v[4:5] op_sel:[0,1] op_sel_hi:[0,1]
	v_pk_add_f32 v[26:27], v[16:17], v[16:17] op_sel:[0,1] op_sel_hi:[0,1] neg_lo:[0,1] neg_hi:[0,1]
	s_mov_b64 s[70:71], 0x5003c0
	s_waitcnt vmcnt(3)
	v_mov_b32_e32 v9, v52
	v_mov_b32_e32 v52, v51
	v_mov_b32_e32 v8, v50
	v_pk_mul_f32 v[4:5], v[28:29], v[52:53]
	s_nop 0
	v_pk_fma_f32 v[4:5], v[26:27], v[8:9], v[4:5] neg_lo:[0,0,1] neg_hi:[0,0,1]
	s_nop 0
	v_pk_add_f32 v[56:57], v[2:3], v[4:5]
	s_waitcnt vmcnt(0)
	v_mov_b32_e32 v3, v72
	v_mov_b32_e32 v72, v71
	v_mov_b32_e32 v2, v70
	v_pk_mul_f32 v[4:5], v[28:29], v[72:73]
	s_nop 0
	v_pk_fma_f32 v[2:3], v[26:27], v[2:3], v[4:5] neg_lo:[0,0,1] neg_hi:[0,0,1]
	s_nop 0
	v_pk_add_f32 v[54:55], v[6:7], v[2:3]
	v_mov_b32_e32 v3, v64
	v_mov_b32_e32 v64, v63
	v_mov_b32_e32 v2, v62
	v_pk_mul_f32 v[4:5], v[28:29], v[64:65]
	s_nop 0
	v_pk_fma_f32 v[2:3], v[26:27], v[2:3], v[4:5] neg_lo:[0,0,1] neg_hi:[0,0,1]
	s_nop 0
	v_pk_add_f32 v[52:53], v[10:11], v[2:3]
	v_mov_b32_e32 v3, v60
	v_mov_b32_e32 v60, v59
	v_mov_b32_e32 v2, v58
	v_pk_mul_f32 v[4:5], v[28:29], v[60:61]
	s_nop 0
	v_pk_fma_f32 v[2:3], v[26:27], v[2:3], v[4:5] neg_lo:[0,0,1] neg_hi:[0,0,1]
	s_nop 0
	v_pk_add_f32 v[50:51], v[14:15], v[2:3]
	v_lshl_add_u64 v[14:15], v[48:49], 0, s[70:71]
	global_load_dwordx4 v[10:13], v[46:47], off offset:960
	global_load_dwordx4 v[2:5], v[14:15], off offset:48
	global_load_dwordx4 v[6:9], v[14:15], off offset:32
	s_nop 0
	global_load_dwordx4 v[14:17], v[14:15], off offset:16
	s_mov_b64 s[70:71], 0x400
	v_lshl_add_u64 v[38:39], v[38:39], 0, s[70:71]
	s_waitcnt vmcnt(3)
	v_mov_b32_e32 v47, v12
	v_mov_b32_e32 v12, v11
	v_mov_b32_e32 v46, v10
	v_pk_mul_f32 v[10:11], v[28:29], v[12:13]
	s_nop 0
	v_pk_fma_f32 v[10:11], v[26:27], v[46:47], v[10:11] neg_lo:[0,0,1] neg_hi:[0,0,1]
	s_nop 0
	v_pk_add_f32 v[58:59], v[24:25], v[10:11]
	s_waitcnt vmcnt(0)
	v_mov_b32_e32 v11, v16
	v_mov_b32_e32 v16, v15
	v_mov_b32_e32 v10, v14
	v_pk_mul_f32 v[12:13], v[28:29], v[16:17]
	s_nop 0
	v_pk_fma_f32 v[10:11], v[26:27], v[10:11], v[12:13] neg_lo:[0,0,1] neg_hi:[0,0,1]
	s_nop 0
	v_pk_add_f32 v[60:61], v[22:23], v[10:11]
	v_mov_b32_e32 v11, v8
	v_mov_b32_e32 v8, v7
	v_mov_b32_e32 v10, v6
	v_pk_mul_f32 v[6:7], v[28:29], v[8:9]
	s_nop 0
	v_pk_fma_f32 v[6:7], v[26:27], v[10:11], v[6:7] neg_lo:[0,0,1] neg_hi:[0,0,1]
	s_nop 0
	v_pk_add_f32 v[64:65], v[20:21], v[6:7]
	v_mov_b32_e32 v7, v4
	v_mov_b32_e32 v4, v3
	v_mov_b32_e32 v6, v2
	v_pk_mul_f32 v[2:3], v[28:29], v[4:5]
	s_nop 0
	v_pk_fma_f32 v[2:3], v[26:27], v[6:7], v[2:3] neg_lo:[0,0,1] neg_hi:[0,0,1]
	s_nop 0
	v_pk_add_f32 v[62:63], v[18:19], v[2:3]
	s_cbranch_scc0 .LBB0_108
	v_and_b32_e32 v2, 31, v69
	v_cmp_eq_u32_e32 vcc, 0, v2
	v_mov_b32_e32 v3, 0
	s_and_saveexec_b64 s[48:49], vcc
	s_cbranch_execz .LBB0_106
	v_lshl_or_b32 v4, v36, 4, v160
	v_readlane_b32 s0, v250, 33
	v_ashrrev_i32_e32 v5, 31, v4
	v_readlane_b32 s14, v250, 47
	v_readlane_b32 s15, v250, 48
	v_readlane_b32 s1, v250, 34
	v_readlane_b32 s2, v250, 35
	v_lshl_add_u64 v[4:5], v[4:5], 2, s[14:15]
	global_load_dword v3, v[4:5], off
	v_readlane_b32 s3, v250, 36
	v_readlane_b32 s4, v250, 37
	v_readlane_b32 s5, v250, 38
	v_readlane_b32 s6, v250, 39
	v_readlane_b32 s7, v250, 40
	v_readlane_b32 s8, v250, 41
	v_readlane_b32 s9, v250, 42
	v_readlane_b32 s10, v250, 43
	v_readlane_b32 s11, v250, 44
	v_readlane_b32 s12, v250, 45
	v_readlane_b32 s13, v250, 46
	s_branch .LBB0_106

; __device__ __forceinline__ void ph1_small(const Args& a, int tid, int wave, int lane, int G, int bid) {
;     ...
; #pragma unroll 8
;             for (int n = 0; n < 64; ++n) { const float cr = cre[((size_t)g * 16 + p) * 64 + n], ci = cim[((size_t)g * 16 + p) * 64 + n];
;                 const float pr = POW[(((size_t)g * 65 + tau) * 64 + n) * 2], pi = POW[(((size_t)g * 65 + tau) * 64 + n) * 2 + 1];
;                 const float er = cr * pr - ci * pi, ei = cr * pi + ci * pr;
;                 const f32x4* bp = (const f32x4*)(BBAR + ((size_t)g * 64 + n) * 32);
; #pragma unroll
;                 for (int q = 0; q < 8; ++q) { const f32x4 bb = bp[q]; s[2 * q] += er * bb[0] - ei * bb[1]; s[2 * q + 1] += er * bb[2] - ei * bb[3]; } }
.LBB0_324:
	s_waitcnt lgkmcnt(0)
	v_lshl_add_u64 v[6:7], v[44:45], 0, s[40:41]
	v_lshl_add_u64 v[10:11], v[42:43], 0, s[40:41]
	global_load_dwordx4 v[2:5], v[6:7], off offset:16
	global_load_dwordx4 v[18:21], v[6:7], off
	s_nop 0
	global_load_dwordx4 v[6:9], v[10:11], off offset:16
	global_load_dwordx4 v[22:25], v[10:11], off
	v_lshl_add_u64 v[10:11], s[74:75], 0, v[40:41]
	s_mov_b64 s[42:43], 0x600000
	s_mov_b32 s33, 0x600000
	v_lshl_add_u64 v[26:27], v[10:11], 0, s[42:43]
	v_add_co_u32_e32 v10, vcc, s33, v10
	v_lshl_add_u64 v[48:49], s[74:75], 0, v[38:39]
	s_nop 0
	v_addc_co_u32_e32 v11, vcc, 0, v11, vcc
	global_load_dwordx4 v[68:71], v[10:11], off
	s_nop 0
	global_load_dwordx4 v[10:13], v[26:27], off offset:48
	global_load_dwordx4 v[14:17], v[26:27], off offset:32
	s_nop 0
	global_load_dwordx4 v[26:29], v[26:27], off offset:16
	s_mov_b32 s33, 0x500000
	s_mov_b64 s[42:43], 0x500000
	v_lshl_add_u64 v[84:85], v[48:49], 0, s[42:43]
	s_mov_b64 s[42:43], 0x500040
	v_readfirstlane_b32 s98, v48
	v_readfirstlane_b32 s99, v49
	s_add_u32 s98, s98, 0x500400
	s_addc_u32 s99, s99, 0
	s_nop 0
	s_load_dword s100, s[98:99], 0x0
	s_load_dword s101, s[98:99], 0x80
	s_load_dword s100, s[98:99], 0x100
	s_load_dword s101, s[98:99], 0x180
	s_load_dword s100, s[98:99], 0x200
	s_load_dword s101, s[98:99], 0x280
	s_load_dword s100, s[98:99], 0x300
	s_load_dword s101, s[98:99], 0x380
	s_add_u32 s40, s40, 32
	s_addc_u32 s41, s41, 0
	v_lshl_add_u64 v[40:41], v[40:41], 0, 64
	s_cmpk_eq_i32 s40, 0x100
	s_waitcnt vmcnt(6)
	v_mov_b32_e32 v46, v18
	s_waitcnt vmcnt(4)
	v_mov_b32_e32 v47, v22
	s_waitcnt vmcnt(3)
	v_pk_mul_f32 v[88:89], v[46:47], v[68:69]
	v_mov_b32_e32 v46, v22
	v_mov_b32_e32 v47, v18
	v_pk_mul_f32 v[68:69], v[46:47], v[68:69]
	v_add_co_u32_e32 v46, vcc, s33, v48
	v_pk_add_f32 v[68:69], v[68:69], v[68:69] op_sel:[0,1] op_sel_hi:[0,1]
	s_nop 0
	v_addc_co_u32_e32 v47, vcc, 0, v49, vcc
	global_load_dwordx4 v[72:75], v[46:47], off
	global_load_dwordx4 v[76:79], v[84:85], off offset:48
	global_load_dwordx4 v[80:83], v[84:85], off offset:32
	s_nop 0
	global_load_dwordx4 v[84:87], v[84:85], off offset:16
	v_pk_add_f32 v[88:89], v[88:89], v[88:89] op_sel:[0,1] op_sel_hi:[0,1] neg_lo:[0,1] neg_hi:[0,1]
	v_mov_b32_e32 v22, v19
	v_mov_b32_e32 v18, v23
	v_pk_mul_f32 v[18:19], v[18:19], v[70:71]
	s_waitcnt vmcnt(3)
	v_mov_b32_e32 v91, v74
	v_mov_b32_e32 v74, v73
	v_mov_b32_e32 v90, v72
	v_pk_mul_f32 v[72:73], v[68:69], v[74:75]
	v_pk_add_f32 v[18:19], v[18:19], v[18:19] op_sel:[0,1] op_sel_hi:[0,1]
	v_pk_fma_f32 v[72:73], v[88:89], v[90:91], v[72:73] neg_lo:[0,0,1] neg_hi:[0,0,1]
	s_nop 0
	v_pk_add_f32 v[90:91], v[56:57], v[72:73]
	s_waitcnt vmcnt(0)
	v_mov_b32_e32 v57, v86
	v_mov_b32_e32 v86, v85
	v_mov_b32_e32 v56, v84
	v_pk_mul_f32 v[72:73], v[68:69], v[86:87]
	s_nop 0
	v_pk_fma_f32 v[56:57], v[88:89], v[56:57], v[72:73] neg_lo:[0,0,1] neg_hi:[0,0,1]
	s_nop 0
	v_pk_add_f32 v[84:85], v[54:55], v[56:57]
	v_mov_b32_e32 v55, v82
	v_mov_b32_e32 v82, v81
	v_mov_b32_e32 v54, v80
	v_pk_mul_f32 v[56:57], v[68:69], v[82:83]
	s_nop 0
	v_pk_fma_f32 v[54:55], v[88:89], v[54:55], v[56:57] neg_lo:[0,0,1] neg_hi:[0,0,1]
	s_nop 0
	v_pk_add_f32 v[80:81], v[52:53], v[54:55]
	v_mov_b32_e32 v53, v78
	v_mov_b32_e32 v78, v77
	v_mov_b32_e32 v52, v76
	v_pk_mul_f32 v[54:55], v[68:69], v[78:79]
	v_lshl_add_u64 v[76:77], v[48:49], 0, s[42:43]
	v_pk_fma_f32 v[52:53], v[88:89], v[52:53], v[54:55] neg_lo:[0,0,1] neg_hi:[0,0,1]
	s_mov_b64 s[42:43], 0x500080
	v_pk_add_f32 v[82:83], v[50:51], v[52:53]
	global_load_dwordx4 v[50:53], v[46:47], off offset:64
	global_load_dwordx4 v[54:57], v[76:77], off offset:48
	global_load_dwordx4 v[72:75], v[76:77], off offset:32
	s_nop 0
	global_load_dwordx4 v[76:79], v[76:77], off offset:16
	s_waitcnt vmcnt(3)
	v_mov_b32_e32 v87, v52
	v_mov_b32_e32 v52, v51
	v_mov_b32_e32 v86, v50
	v_pk_mul_f32 v[50:51], v[68:69], v[52:53]
	s_nop 0
	v_pk_fma_f32 v[50:51], v[88:89], v[86:87], v[50:51] neg_lo:[0,0,1] neg_hi:[0,0,1]
	s_nop 0
	v_pk_add_f32 v[86:87], v[58:59], v[50:51]
	s_waitcnt vmcnt(0)
	v_mov_b32_e32 v51, v78
	v_mov_b32_e32 v78, v77
	v_mov_b32_e32 v50, v76
	v_pk_mul_f32 v[52:53], v[68:69], v[78:79]
	s_nop 0
	v_pk_fma_f32 v[50:51], v[88:89], v[50:51], v[52:53] neg_lo:[0,0,1] neg_hi:[0,0,1]
	s_nop 0
	v_pk_add_f32 v[76:77], v[60:61], v[50:51]
	v_mov_b32_e32 v51, v74
	v_mov_b32_e32 v74, v73
	v_mov_b32_e32 v50, v72
	v_pk_mul_f32 v[52:53], v[68:69], v[74:75]
	v_pk_mul_f32 v[74:75], v[22:23], v[70:71]
	v_pk_fma_f32 v[50:51], v[88:89], v[50:51], v[52:53] neg_lo:[0,0,1] neg_hi:[0,0,1]
	v_lshl_add_u64 v[22:23], v[48:49], 0, s[42:43]
	v_pk_add_f32 v[72:73], v[64:65], v[50:51]
	v_mov_b32_e32 v51, v56
	v_mov_b32_e32 v56, v55
	v_mov_b32_e32 v50, v54
	v_pk_mul_f32 v[52:53], v[68:69], v[56:57]
	s_mov_b64 s[42:43], 0x5000c0
	v_pk_fma_f32 v[50:51], v[88:89], v[50:51], v[52:53] neg_lo:[0,0,1] neg_hi:[0,0,1]
	s_nop 0
	v_pk_add_f32 v[68:69], v[62:63], v[50:51]
	global_load_dwordx4 v[50:53], v[46:47], off offset:128
	global_load_dwordx4 v[54:57], v[22:23], off offset:48
	global_load_dwordx4 v[58:61], v[22:23], off offset:32
	global_load_dwordx4 v[62:65], v[22:23], off offset:16
	v_pk_add_f32 v[22:23], v[74:75], v[74:75] op_sel:[0,1] op_sel_hi:[0,1] neg_lo:[0,1] neg_hi:[0,1]
	s_waitcnt vmcnt(3)
	v_mov_b32_e32 v71, v52
	v_mov_b32_e32 v52, v51
	v_mov_b32_e32 v70, v50
	v_pk_mul_f32 v[50:51], v[18:19], v[52:53]
	s_nop 0
	v_pk_fma_f32 v[50:51], v[22:23], v[70:71], v[50:51] neg_lo:[0,0,1] neg_hi:[0,0,1]
	s_nop 0
	v_pk_add_f32 v[88:89], v[90:91], v[50:51]
	s_waitcnt vmcnt(0)
; __device__ __forceinline__ void ph1_small(const Args& a, int tid, int wave, int lane, int G, int bid) {
;     ...
;             for (int n = 0; n < 64; ++n) { const float cr = cre[((size_t)g * 16 + p) * 64 + n], ci = cim[((size_t)g * 16 + p) * 64 + n];
;                 const float pr = POW[(((size_t)g * 65 + tau) * 64 + n) * 2], pi = POW[(((size_t)g * 65 + tau) * 64 + n) * 2 + 1];
;                 const float er = cr * pr - ci * pi, ei = cr * pi + ci * pr;
;                 const f32x4* bp = (const f32x4*)(BBAR + ((size_t)g * 64 + n) * 32);
; #pragma unroll
;                 for (int q = 0; q < 8; ++q) { const f32x4 bb = bp[q]; s[2 * q] += er * bb[0] - ei * bb[1]; s[2 * q + 1] += er * bb[2] - ei * bb[3]; } }
	v_mov_b32_e32 v51, v64
	v_mov_b32_e32 v64, v63
	v_mov_b32_e32 v50, v62
	v_pk_mul_f32 v[52:53], v[18:19], v[64:65]
	s_nop 0
	v_pk_fma_f32 v[50:51], v[22:23], v[50:51], v[52:53] neg_lo:[0,0,1] neg_hi:[0,0,1]
	s_nop 0
	v_pk_add_f32 v[84:85], v[84:85], v[50:51]
	v_mov_b32_e32 v51, v60
	v_mov_b32_e32 v60, v59
	v_mov_b32_e32 v50, v58
	v_pk_mul_f32 v[52:53], v[18:19], v[60:61]
	s_nop 0
	v_pk_fma_f32 v[50:51], v[22:23], v[50:51], v[52:53] neg_lo:[0,0,1] neg_hi:[0,0,1]
	s_nop 0
	v_pk_add_f32 v[90:91], v[80:81], v[50:51]
	v_mov_b32_e32 v51, v56
	v_mov_b32_e32 v56, v55
	v_mov_b32_e32 v50, v54
	v_pk_mul_f32 v[52:53], v[18:19], v[56:57]
	v_lshl_add_u64 v[54:55], v[48:49], 0, s[42:43]
	v_pk_fma_f32 v[50:51], v[22:23], v[50:51], v[52:53] neg_lo:[0,0,1] neg_hi:[0,0,1]
	s_mov_b64 s[42:43], 0x500100
	v_pk_add_f32 v[92:93], v[82:83], v[50:51]
	global_load_dwordx4 v[50:53], v[46:47], off offset:192
	global_load_dwordx4 v[58:61], v[54:55], off offset:48
	global_load_dwordx4 v[62:65], v[54:55], off offset:32
	s_nop 0
	global_load_dwordx4 v[54:57], v[54:55], off offset:16
	s_waitcnt vmcnt(3)
	v_mov_b32_e32 v71, v52
	v_mov_b32_e32 v52, v51
	v_mov_b32_e32 v70, v50
	v_pk_mul_f32 v[50:51], v[18:19], v[52:53]
	s_nop 0
	v_pk_fma_f32 v[50:51], v[22:23], v[70:71], v[50:51] neg_lo:[0,0,1] neg_hi:[0,0,1]
	s_nop 0
	v_pk_add_f32 v[52:53], v[86:87], v[50:51]
	s_waitcnt vmcnt(0)
	v_mov_b32_e32 v51, v56
	v_mov_b32_e32 v56, v55
	v_mov_b32_e32 v50, v54
	v_pk_mul_f32 v[54:55], v[18:19], v[56:57]
	s_nop 0
	v_pk_fma_f32 v[50:51], v[22:23], v[50:51], v[54:55] neg_lo:[0,0,1] neg_hi:[0,0,1]
	s_nop 0
	v_pk_add_f32 v[54:55], v[76:77], v[50:51]
	v_mov_b32_e32 v51, v64
	v_mov_b32_e32 v64, v63
	v_mov_b32_e32 v50, v62
	v_pk_mul_f32 v[56:57], v[18:19], v[64:65]
	s_nop 0
	v_pk_fma_f32 v[50:51], v[22:23], v[50:51], v[56:57] neg_lo:[0,0,1] neg_hi:[0,0,1]
	s_nop 0
	v_pk_add_f32 v[56:57], v[72:73], v[50:51]
	v_mov_b32_e32 v51, v60
	v_mov_b32_e32 v60, v59
	v_mov_b32_e32 v50, v58
	v_pk_mul_f32 v[18:19], v[18:19], v[60:61]
	s_nop 0
	v_pk_fma_f32 v[18:19], v[22:23], v[50:51], v[18:19] neg_lo:[0,0,1] neg_hi:[0,0,1]
	v_mov_b32_e32 v22, v24
	v_pk_add_f32 v[58:59], v[68:69], v[18:19]
	v_mov_b32_e32 v18, v20
	v_mov_b32_e32 v19, v24
	v_mov_b32_e32 v23, v20
	v_pk_mul_f32 v[18:19], v[18:19], v[26:27]
	v_pk_mul_f32 v[22:23], v[22:23], v[26:27]
	v_lshl_add_u64 v[26:27], v[48:49], 0, s[42:43]
	global_load_dwordx4 v[68:71], v[46:47], off offset:256
	global_load_dwordx4 v[72:75], v[26:27], off offset:48
	global_load_dwordx4 v[76:79], v[26:27], off offset:32
	global_load_dwordx4 v[80:83], v[26:27], off offset:16
	v_pk_add_f32 v[60:61], v[18:19], v[18:19] op_sel:[0,1] op_sel_hi:[0,1] neg_lo:[0,1] neg_hi:[0,1]
	v_pk_add_f32 v[62:63], v[22:23], v[22:23] op_sel:[0,1] op_sel_hi:[0,1]
	s_mov_b64 s[42:43], 0x500140
	v_mov_b32_e32 v24, v21
	v_mov_b32_e32 v20, v25
	v_pk_mul_f32 v[20:21], v[20:21], v[28:29]
	s_waitcnt vmcnt(3)
	v_mov_b32_e32 v19, v70
	v_mov_b32_e32 v70, v69
	v_mov_b32_e32 v18, v68
	v_pk_mul_f32 v[22:23], v[62:63], v[70:71]
	s_nop 0
	v_pk_fma_f32 v[18:19], v[60:61], v[18:19], v[22:23] neg_lo:[0,0,1] neg_hi:[0,0,1]
	s_waitcnt vmcnt(0)
	v_mov_b32_e32 v23, v82
	v_mov_b32_e32 v82, v81
	v_mov_b32_e32 v22, v80
	v_pk_mul_f32 v[26:27], v[62:63], v[82:83]
	v_pk_add_f32 v[18:19], v[88:89], v[18:19]
	v_pk_fma_f32 v[22:23], v[60:61], v[22:23], v[26:27] neg_lo:[0,0,1] neg_hi:[0,0,1]
	v_mov_b32_e32 v27, v78
	v_mov_b32_e32 v78, v77
	v_mov_b32_e32 v26, v76
	v_pk_mul_f32 v[50:51], v[62:63], v[78:79]
	v_pk_add_f32 v[22:23], v[84:85], v[22:23]
	v_pk_fma_f32 v[26:27], v[60:61], v[26:27], v[50:51] neg_lo:[0,0,1] neg_hi:[0,0,1]
	v_mov_b32_e32 v51, v74
	v_mov_b32_e32 v74, v73
	v_mov_b32_e32 v50, v72
	v_pk_mul_f32 v[64:65], v[62:63], v[74:75]
	v_pk_add_f32 v[26:27], v[90:91], v[26:27]
	v_pk_fma_f32 v[50:51], v[60:61], v[50:51], v[64:65] neg_lo:[0,0,1] neg_hi:[0,0,1]
	v_lshl_add_u64 v[64:65], v[48:49], 0, s[42:43]
	global_load_dwordx4 v[68:71], v[46:47], off offset:320
	global_load_dwordx4 v[72:75], v[64:65], off offset:48
	global_load_dwordx4 v[76:79], v[64:65], off offset:32
	global_load_dwordx4 v[80:83], v[64:65], off offset:16
	s_mov_b64 s[42:43], 0x500180
	v_pk_add_f32 v[50:51], v[92:93], v[50:51]
	s_waitcnt vmcnt(3)
	v_mov_b32_e32 v65, v70
	v_mov_b32_e32 v70, v69
	v_mov_b32_e32 v64, v68
	v_pk_mul_f32 v[68:69], v[62:63], v[70:71]
	s_nop 0
	v_pk_fma_f32 v[64:65], v[60:61], v[64:65], v[68:69] neg_lo:[0,0,1] neg_hi:[0,0,1]
	s_nop 0
	v_pk_add_f32 v[64:65], v[52:53], v[64:65]
	s_waitcnt vmcnt(0)
	v_mov_b32_e32 v53, v82
	v_mov_b32_e32 v82, v81
	v_mov_b32_e32 v52, v80
	v_pk_mul_f32 v[68:69], v[62:63], v[82:83]
	v_pk_add_f32 v[82:83], v[20:21], v[20:21] op_sel:[0,1] op_sel_hi:[0,1]
	v_pk_fma_f32 v[52:53], v[60:61], v[52:53], v[68:69] neg_lo:[0,0,1] neg_hi:[0,0,1]
	s_nop 0
	v_pk_add_f32 v[54:55], v[54:55], v[52:53]
	v_mov_b32_e32 v53, v78
	v_mov_b32_e32 v78, v77
	v_mov_b32_e32 v52, v76
	v_pk_mul_f32 v[68:69], v[62:63], v[78:79]
	s_nop 0
	v_pk_fma_f32 v[52:53], v[60:61], v[52:53], v[68:69] neg_lo:[0,0,1] neg_hi:[0,0,1]
	s_nop 0
	v_pk_add_f32 v[56:57], v[56:57], v[52:53]
	v_mov_b32_e32 v53, v74
	v_mov_b32_e32 v74, v73
	v_mov_b32_e32 v52, v72
	v_pk_mul_f32 v[62:63], v[62:63], v[74:75]
	s_nop 0
	v_pk_fma_f32 v[52:53], v[60:61], v[52:53], v[62:63] neg_lo:[0,0,1] neg_hi:[0,0,1]
	s_nop 0
	v_pk_add_f32 v[58:59], v[58:59], v[52:53]
	v_pk_mul_f32 v[52:53], v[24:25], v[28:29]
	v_lshl_add_u64 v[24:25], v[48:49], 0, s[42:43]
	global_load_dwordx4 v[60:63], v[46:47], off offset:384
	global_load_dwordx4 v[68:71], v[24:25], off offset:48
	global_load_dwordx4 v[72:75], v[24:25], off offset:32
	global_load_dwordx4 v[76:79], v[24:25], off offset:16
	v_pk_add_f32 v[80:81], v[52:53], v[52:53] op_sel:[0,1] op_sel_hi:[0,1] neg_lo:[0,1] neg_hi:[0,1]
	s_mov_b64 s[42:43], 0x5001c0
	s_waitcnt vmcnt(3)
; __device__ __forceinline__ void ph1_small(const Args& a, int tid, int wave, int lane, int G, int bid) {
;     ...
;             for (int n = 0; n < 64; ++n) { const float cr = cre[((size_t)g * 16 + p) * 64 + n], ci = cim[((size_t)g * 16 + p) * 64 + n];
;                 const float pr = POW[(((size_t)g * 65 + tau) * 64 + n) * 2], pi = POW[(((size_t)g * 65 + tau) * 64 + n) * 2 + 1];
;                 const float er = cr * pr - ci * pi, ei = cr * pi + ci * pr;
;                 const f32x4* bp = (const f32x4*)(BBAR + ((size_t)g * 64 + n) * 32);
; #pragma unroll
;                 for (int q = 0; q < 8; ++q) { const f32x4 bb = bp[q]; s[2 * q] += er * bb[0] - ei * bb[1]; s[2 * q + 1] += er * bb[2] - ei * bb[3]; } }
	v_mov_b32_e32 v25, v62
	v_mov_b32_e32 v62, v61
	v_mov_b32_e32 v24, v60
	v_pk_mul_f32 v[20:21], v[82:83], v[62:63]
	s_nop 0
	v_pk_fma_f32 v[20:21], v[80:81], v[24:25], v[20:21] neg_lo:[0,0,1] neg_hi:[0,0,1]
	s_nop 0
	v_pk_add_f32 v[28:29], v[18:19], v[20:21]
	s_waitcnt vmcnt(0)
	v_mov_b32_e32 v19, v78
	v_mov_b32_e32 v78, v77
	v_mov_b32_e32 v18, v76
	v_pk_mul_f32 v[20:21], v[82:83], v[78:79]
	s_nop 0
	v_pk_fma_f32 v[18:19], v[80:81], v[18:19], v[20:21] neg_lo:[0,0,1] neg_hi:[0,0,1]
	s_nop 0
	v_pk_add_f32 v[52:53], v[22:23], v[18:19]
	v_mov_b32_e32 v19, v74
	v_mov_b32_e32 v74, v73
	v_mov_b32_e32 v18, v72
	v_pk_mul_f32 v[20:21], v[82:83], v[74:75]
	s_nop 0
	v_pk_fma_f32 v[18:19], v[80:81], v[18:19], v[20:21] neg_lo:[0,0,1] neg_hi:[0,0,1]
	s_nop 0
	v_pk_add_f32 v[26:27], v[26:27], v[18:19]
	v_mov_b32_e32 v19, v70
	v_mov_b32_e32 v70, v69
	v_mov_b32_e32 v18, v68
	v_pk_mul_f32 v[20:21], v[82:83], v[70:71]
	v_lshl_add_u64 v[68:69], v[48:49], 0, s[42:43]
	v_pk_fma_f32 v[18:19], v[80:81], v[18:19], v[20:21] neg_lo:[0,0,1] neg_hi:[0,0,1]
	s_mov_b64 s[42:43], 0x500200
	v_pk_add_f32 v[50:51], v[50:51], v[18:19]
	global_load_dwordx4 v[18:21], v[46:47], off offset:448
	global_load_dwordx4 v[60:63], v[68:69], off offset:48
	global_load_dwordx4 v[22:25], v[68:69], off offset:32
	s_nop 0
	global_load_dwordx4 v[68:71], v[68:69], off offset:16
	s_waitcnt vmcnt(3)
	v_mov_b32_e32 v73, v20
	v_mov_b32_e32 v20, v19
	v_mov_b32_e32 v72, v18
	v_pk_mul_f32 v[18:19], v[82:83], v[20:21]
	s_waitcnt vmcnt(0)
	v_mov_b32_e32 v21, v70
	v_pk_fma_f32 v[18:19], v[80:81], v[72:73], v[18:19] neg_lo:[0,0,1] neg_hi:[0,0,1]
	v_mov_b32_e32 v70, v69
	v_pk_add_f32 v[18:19], v[64:65], v[18:19]
	v_mov_b32_e32 v20, v68
	v_pk_mul_f32 v[64:65], v[82:83], v[70:71]
	v_lshl_add_u64 v[68:69], v[48:49], 0, s[42:43]
	v_pk_fma_f32 v[20:21], v[80:81], v[20:21], v[64:65] neg_lo:[0,0,1] neg_hi:[0,0,1]
	s_mov_b64 s[42:43], 0x500240
	v_pk_add_f32 v[20:21], v[54:55], v[20:21]
	v_mov_b32_e32 v55, v24
	v_mov_b32_e32 v24, v23
	v_mov_b32_e32 v54, v22
	v_pk_mul_f32 v[22:23], v[82:83], v[24:25]
	v_mov_b32_e32 v25, v62
	v_mov_b32_e32 v62, v61
	v_pk_fma_f32 v[22:23], v[80:81], v[54:55], v[22:23] neg_lo:[0,0,1] neg_hi:[0,0,1]
	v_mov_b32_e32 v24, v60
	v_pk_mul_f32 v[54:55], v[82:83], v[62:63]
	v_pk_add_f32 v[22:23], v[56:57], v[22:23]
	v_pk_fma_f32 v[24:25], v[80:81], v[24:25], v[54:55] neg_lo:[0,0,1] neg_hi:[0,0,1]
	v_mov_b32_e32 v54, v2
	v_mov_b32_e32 v55, v6
	v_pk_mul_f32 v[72:73], v[54:55], v[14:15]
	v_mov_b32_e32 v54, v6
	v_mov_b32_e32 v55, v2
	v_pk_add_f32 v[24:25], v[58:59], v[24:25]
	v_pk_mul_f32 v[14:15], v[54:55], v[14:15]
	global_load_dwordx4 v[54:57], v[46:47], off offset:512
	global_load_dwordx4 v[58:61], v[68:69], off offset:48
	global_load_dwordx4 v[62:65], v[68:69], off offset:32
	s_nop 0
	global_load_dwordx4 v[68:71], v[68:69], off offset:16
	v_pk_add_f32 v[76:77], v[14:15], v[14:15] op_sel:[0,1] op_sel_hi:[0,1]
	v_pk_add_f32 v[72:73], v[72:73], v[72:73] op_sel:[0,1] op_sel_hi:[0,1] neg_lo:[0,1] neg_hi:[0,1]
	v_mov_b32_e32 v6, v3
	v_mov_b32_e32 v2, v7
	v_pk_mul_f32 v[2:3], v[2:3], v[16:17]
	s_waitcnt vmcnt(3)
	v_mov_b32_e32 v75, v56
	v_mov_b32_e32 v56, v55
	v_mov_b32_e32 v74, v54
	v_pk_mul_f32 v[14:15], v[76:77], v[56:57]
	s_nop 0
	v_pk_fma_f32 v[14:15], v[72:73], v[74:75], v[14:15] neg_lo:[0,0,1] neg_hi:[0,0,1]
	s_nop 0
	v_pk_add_f32 v[14:15], v[28:29], v[14:15]
	s_waitcnt vmcnt(0)
	v_mov_b32_e32 v29, v70
	v_mov_b32_e32 v70, v69
	v_mov_b32_e32 v28, v68
	v_pk_mul_f32 v[54:55], v[76:77], v[70:71]
	s_nop 0
	v_pk_fma_f32 v[28:29], v[72:73], v[28:29], v[54:55] neg_lo:[0,0,1] neg_hi:[0,0,1]
	s_nop 0
	v_pk_add_f32 v[28:29], v[52:53], v[28:29]
	v_mov_b32_e32 v53, v64
	v_mov_b32_e32 v64, v63
	v_mov_b32_e32 v52, v62
	v_pk_mul_f32 v[54:55], v[76:77], v[64:65]
	v_lshl_add_u64 v[64:65], v[48:49], 0, s[42:43]
	v_pk_fma_f32 v[52:53], v[72:73], v[52:53], v[54:55] neg_lo:[0,0,1] neg_hi:[0,0,1]
	s_mov_b64 s[42:43], 0x500280
	v_pk_add_f32 v[26:27], v[26:27], v[52:53]
	v_mov_b32_e32 v53, v60
	v_mov_b32_e32 v60, v59
	v_mov_b32_e32 v52, v58
	v_pk_mul_f32 v[54:55], v[76:77], v[60:61]
	s_nop 0
	v_pk_fma_f32 v[52:53], v[72:73], v[52:53], v[54:55] neg_lo:[0,0,1] neg_hi:[0,0,1]
	s_nop 0
	v_pk_add_f32 v[50:51], v[50:51], v[52:53]
	global_load_dwordx4 v[52:55], v[46:47], off offset:576
	global_load_dwordx4 v[56:59], v[64:65], off offset:48
	global_load_dwordx4 v[60:63], v[64:65], off offset:32
	global_load_dwordx4 v[68:71], v[64:65], off offset:16
	s_waitcnt vmcnt(3)
	v_mov_b32_e32 v65, v54
	v_mov_b32_e32 v54, v53
	v_mov_b32_e32 v64, v52
	v_pk_mul_f32 v[52:53], v[76:77], v[54:55]
	s_nop 0
	v_pk_fma_f32 v[52:53], v[72:73], v[64:65], v[52:53] neg_lo:[0,0,1] neg_hi:[0,0,1]
	v_pk_mul_f32 v[64:65], v[6:7], v[16:17]
	v_pk_add_f32 v[18:19], v[18:19], v[52:53]
	s_waitcnt vmcnt(0)
	v_mov_b32_e32 v53, v70
	v_mov_b32_e32 v70, v69
	v_mov_b32_e32 v52, v68
	v_pk_mul_f32 v[54:55], v[76:77], v[70:71]
	v_lshl_add_u64 v[6:7], v[48:49], 0, s[42:43]
	v_pk_fma_f32 v[52:53], v[72:73], v[52:53], v[54:55] neg_lo:[0,0,1] neg_hi:[0,0,1]
	v_pk_add_f32 v[64:65], v[64:65], v[64:65] op_sel:[0,1] op_sel_hi:[0,1] neg_lo:[0,1] neg_hi:[0,1]
	v_pk_add_f32 v[20:21], v[20:21], v[52:53]
	v_mov_b32_e32 v53, v62
	v_mov_b32_e32 v62, v61
	v_mov_b32_e32 v52, v60
	v_pk_mul_f32 v[54:55], v[76:77], v[62:63]
	s_mov_b64 s[42:43], 0x5002c0
	v_pk_fma_f32 v[52:53], v[72:73], v[52:53], v[54:55] neg_lo:[0,0,1] neg_hi:[0,0,1]
	s_nop 0
	v_pk_add_f32 v[22:23], v[22:23], v[52:53]
	v_mov_b32_e32 v53, v58
	v_mov_b32_e32 v58, v57
	v_mov_b32_e32 v52, v56
	v_pk_mul_f32 v[54:55], v[76:77], v[58:59]
	s_nop 0
	v_pk_fma_f32 v[52:53], v[72:73], v[52:53], v[54:55] neg_lo:[0,0,1] neg_hi:[0,0,1]
	v_pk_add_f32 v[72:73], v[2:3], v[2:3] op_sel:[0,1] op_sel_hi:[0,1]
	v_pk_add_f32 v[24:25], v[24:25], v[52:53]
	global_load_dwordx4 v[52:55], v[46:47], off offset:640
	global_load_dwordx4 v[56:59], v[6:7], off offset:48
	global_load_dwordx4 v[60:63], v[6:7], off offset:32
	global_load_dwordx4 v[68:71], v[6:7], off offset:16
	s_waitcnt vmcnt(3)
; __device__ __forceinline__ void ph1_small(const Args& a, int tid, int wave, int lane, int G, int bid) {
;     ...
; #pragma unroll 8
;             for (int n = 0; n < 64; ++n) { const float cr = cre[((size_t)g * 16 + p) * 64 + n], ci = cim[((size_t)g * 16 + p) * 64 + n];
;                 const float pr = POW[(((size_t)g * 65 + tau) * 64 + n) * 2], pi = POW[(((size_t)g * 65 + tau) * 64 + n) * 2 + 1];
;                 const float er = cr * pr - ci * pi, ei = cr * pi + ci * pr;
;                 const f32x4* bp = (const f32x4*)(BBAR + ((size_t)g * 64 + n) * 32);
; #pragma unroll
;                 for (int q = 0; q < 8; ++q) { const f32x4 bb = bp[q]; s[2 * q] += er * bb[0] - ei * bb[1]; s[2 * q + 1] += er * bb[2] - ei * bb[3]; } }
	v_mov_b32_e32 v7, v54
	v_mov_b32_e32 v54, v53
	v_mov_b32_e32 v6, v52
	v_pk_mul_f32 v[2:3], v[72:73], v[54:55]
	s_nop 0
	v_pk_fma_f32 v[2:3], v[64:65], v[6:7], v[2:3] neg_lo:[0,0,1] neg_hi:[0,0,1]
	s_waitcnt vmcnt(0)
	v_mov_b32_e32 v7, v70
	v_mov_b32_e32 v70, v69
	v_pk_add_f32 v[2:3], v[14:15], v[2:3]
	v_mov_b32_e32 v6, v68
	v_pk_mul_f32 v[14:15], v[72:73], v[70:71]
	s_nop 0
	v_pk_fma_f32 v[6:7], v[64:65], v[6:7], v[14:15] neg_lo:[0,0,1] neg_hi:[0,0,1]
	v_mov_b32_e32 v15, v62
	v_mov_b32_e32 v62, v61
	v_mov_b32_e32 v14, v60
	v_pk_mul_f32 v[16:17], v[72:73], v[62:63]
	v_pk_add_f32 v[6:7], v[28:29], v[6:7]
	v_pk_fma_f32 v[14:15], v[64:65], v[14:15], v[16:17] neg_lo:[0,0,1] neg_hi:[0,0,1]
	v_mov_b32_e32 v17, v58
	v_mov_b32_e32 v58, v57
	v_pk_add_f32 v[14:15], v[26:27], v[14:15]
	v_mov_b32_e32 v16, v56
	v_pk_mul_f32 v[26:27], v[72:73], v[58:59]
	v_lshl_add_u64 v[58:59], v[48:49], 0, s[42:43]
	v_pk_fma_f32 v[16:17], v[64:65], v[16:17], v[26:27] neg_lo:[0,0,1] neg_hi:[0,0,1]
	s_mov_b64 s[42:43], 0x500300
	v_pk_add_f32 v[16:17], v[50:51], v[16:17]
	global_load_dwordx4 v[26:29], v[46:47], off offset:704
	global_load_dwordx4 v[50:53], v[58:59], off offset:48
	global_load_dwordx4 v[54:57], v[58:59], off offset:32
	s_nop 0
	global_load_dwordx4 v[58:61], v[58:59], off offset:16
	s_waitcnt vmcnt(3)
	v_mov_b32_e32 v63, v28
	v_mov_b32_e32 v28, v27
	v_mov_b32_e32 v62, v26
	v_pk_mul_f32 v[26:27], v[72:73], v[28:29]
	s_nop 0
	v_pk_fma_f32 v[26:27], v[64:65], v[62:63], v[26:27] neg_lo:[0,0,1] neg_hi:[0,0,1]
	s_nop 0
	v_pk_add_f32 v[18:19], v[18:19], v[26:27]
	s_waitcnt vmcnt(0)
	v_mov_b32_e32 v27, v60
	v_mov_b32_e32 v60, v59
	v_mov_b32_e32 v26, v58
	v_pk_mul_f32 v[28:29], v[72:73], v[60:61]
	v_lshl_add_u64 v[58:59], v[48:49], 0, s[42:43]
	v_pk_fma_f32 v[26:27], v[64:65], v[26:27], v[28:29] neg_lo:[0,0,1] neg_hi:[0,0,1]
	s_mov_b64 s[42:43], 0x500340
	v_pk_add_f32 v[20:21], v[20:21], v[26:27]
	v_mov_b32_e32 v27, v56
	v_mov_b32_e32 v56, v55
	v_mov_b32_e32 v26, v54
	v_pk_mul_f32 v[28:29], v[72:73], v[56:57]
	s_nop 0
	v_pk_fma_f32 v[26:27], v[64:65], v[26:27], v[28:29] neg_lo:[0,0,1] neg_hi:[0,0,1]
	s_nop 0
	v_pk_add_f32 v[26:27], v[22:23], v[26:27]
	v_mov_b32_e32 v23, v52
	v_mov_b32_e32 v52, v51
	v_mov_b32_e32 v22, v50
	v_pk_mul_f32 v[28:29], v[72:73], v[52:53]
	s_nop 0
	v_pk_fma_f32 v[22:23], v[64:65], v[22:23], v[28:29] neg_lo:[0,0,1] neg_hi:[0,0,1]
	s_nop 0
	v_pk_add_f32 v[28:29], v[24:25], v[22:23]
	v_mov_b32_e32 v22, v4
	v_mov_b32_e32 v23, v8
	v_pk_mul_f32 v[62:63], v[22:23], v[10:11]
	v_mov_b32_e32 v22, v8
	v_mov_b32_e32 v23, v4
	v_pk_mul_f32 v[10:11], v[22:23], v[10:11]
	global_load_dwordx4 v[22:25], v[46:47], off offset:768
	global_load_dwordx4 v[50:53], v[58:59], off offset:48
	global_load_dwordx4 v[54:57], v[58:59], off offset:32
	s_nop 0
	global_load_dwordx4 v[58:61], v[58:59], off offset:16
	v_pk_add_f32 v[68:69], v[10:11], v[10:11] op_sel:[0,1] op_sel_hi:[0,1]
	v_pk_add_f32 v[62:63], v[62:63], v[62:63] op_sel:[0,1] op_sel_hi:[0,1] neg_lo:[0,1] neg_hi:[0,1]
	v_mov_b32_e32 v8, v5
	v_mov_b32_e32 v4, v9
	v_pk_mul_f32 v[4:5], v[4:5], v[12:13]
	s_waitcnt vmcnt(3)
	v_mov_b32_e32 v65, v24
	v_mov_b32_e32 v24, v23
	v_mov_b32_e32 v64, v22
	v_pk_mul_f32 v[10:11], v[68:69], v[24:25]
	s_nop 0
	v_pk_fma_f32 v[10:11], v[62:63], v[64:65], v[10:11] neg_lo:[0,0,1] neg_hi:[0,0,1]
	s_nop 0
	v_pk_add_f32 v[2:3], v[2:3], v[10:11]
	s_waitcnt vmcnt(0)
	v_mov_b32_e32 v11, v60
	v_mov_b32_e32 v60, v59
	v_mov_b32_e32 v10, v58
	v_pk_mul_f32 v[22:23], v[68:69], v[60:61]
	s_nop 0
	v_pk_fma_f32 v[10:11], v[62:63], v[10:11], v[22:23] neg_lo:[0,0,1] neg_hi:[0,0,1]
	s_nop 0
	v_pk_add_f32 v[6:7], v[6:7], v[10:11]
	v_mov_b32_e32 v11, v56
	v_mov_b32_e32 v56, v55
	v_mov_b32_e32 v10, v54
	v_pk_mul_f32 v[22:23], v[68:69], v[56:57]
	s_nop 0
	v_pk_fma_f32 v[10:11], v[62:63], v[10:11], v[22:23] neg_lo:[0,0,1] neg_hi:[0,0,1]
	s_nop 0
	v_pk_add_f32 v[10:11], v[14:15], v[10:11]
	v_mov_b32_e32 v15, v52
	v_mov_b32_e32 v52, v51
	v_mov_b32_e32 v14, v50
	v_pk_mul_f32 v[22:23], v[68:69], v[52:53]
	s_nop 0
	v_pk_fma_f32 v[14:15], v[62:63], v[14:15], v[22:23] neg_lo:[0,0,1] neg_hi:[0,0,1]
	s_nop 0
	v_pk_add_f32 v[14:15], v[16:17], v[14:15]
	v_lshl_add_u64 v[16:17], v[48:49], 0, s[42:43]
	global_load_dwordx4 v[22:25], v[46:47], off offset:832
	global_load_dwordx4 v[50:53], v[16:17], off offset:48
	global_load_dwordx4 v[54:57], v[16:17], off offset:32
	global_load_dwordx4 v[58:61], v[16:17], off offset:16
	s_mov_b64 s[42:43], 0x500380
	s_waitcnt vmcnt(3)
	v_mov_b32_e32 v17, v24
	v_mov_b32_e32 v24, v23
	v_mov_b32_e32 v16, v22
	v_pk_mul_f32 v[22:23], v[68:69], v[24:25]
	s_nop 0
	v_pk_fma_f32 v[16:17], v[62:63], v[16:17], v[22:23] neg_lo:[0,0,1] neg_hi:[0,0,1]
	s_nop 0
	v_pk_add_f32 v[24:25], v[18:19], v[16:17]
	s_waitcnt vmcnt(0)
; __device__ __forceinline__ void ph1_small(const Args& a, int tid, int wave, int lane, int G, int bid) {
;     ...
;             for (int n = 0; n < 64; ++n) { const float cr = cre[((size_t)g * 16 + p) * 64 + n], ci = cim[((size_t)g * 16 + p) * 64 + n];
;                 const float pr = POW[(((size_t)g * 65 + tau) * 64 + n) * 2], pi = POW[(((size_t)g * 65 + tau) * 64 + n) * 2 + 1];
;                 const float er = cr * pr - ci * pi, ei = cr * pi + ci * pr;
;                 const f32x4* bp = (const f32x4*)(BBAR + ((size_t)g * 64 + n) * 32);
; #pragma unroll
;                 for (int q = 0; q < 8; ++q) { const f32x4 bb = bp[q]; s[2 * q] += er * bb[0] - ei * bb[1]; s[2 * q + 1] += er * bb[2] - ei * bb[3]; } }
;             { const float dv = (tau == 0) ? a.in[I_SD][g * 16 + p] : 0.0f;
; #pragma unroll
;               for (int q = 0; q < 16; ++q) s[q] += (q == p) ? dv : 0.0f; }
	v_mov_b32_e32 v17, v60
	v_mov_b32_e32 v60, v59
	v_mov_b32_e32 v16, v58
	v_pk_mul_f32 v[18:19], v[68:69], v[60:61]
	s_nop 0
	v_pk_fma_f32 v[16:17], v[62:63], v[16:17], v[18:19] neg_lo:[0,0,1] neg_hi:[0,0,1]
	s_nop 0
	v_pk_add_f32 v[22:23], v[20:21], v[16:17]
	v_mov_b32_e32 v17, v56
	v_mov_b32_e32 v56, v55
	v_mov_b32_e32 v16, v54
	v_pk_mul_f32 v[18:19], v[68:69], v[56:57]
	s_nop 0
	v_pk_fma_f32 v[16:17], v[62:63], v[16:17], v[18:19] neg_lo:[0,0,1] neg_hi:[0,0,1]
	s_nop 0
	v_pk_add_f32 v[20:21], v[26:27], v[16:17]
	v_mov_b32_e32 v17, v52
	v_mov_b32_e32 v52, v51
	v_mov_b32_e32 v16, v50
	v_pk_mul_f32 v[18:19], v[68:69], v[52:53]
	s_nop 0
	v_pk_fma_f32 v[16:17], v[62:63], v[16:17], v[18:19] neg_lo:[0,0,1] neg_hi:[0,0,1]
	s_nop 0
	v_pk_add_f32 v[18:19], v[28:29], v[16:17]
	v_pk_mul_f32 v[16:17], v[8:9], v[12:13]
	v_lshl_add_u64 v[8:9], v[48:49], 0, s[42:43]
	global_load_dwordx4 v[50:53], v[46:47], off offset:896
	global_load_dwordx4 v[58:61], v[8:9], off offset:48
	global_load_dwordx4 v[62:65], v[8:9], off offset:32
	global_load_dwordx4 v[68:71], v[8:9], off offset:16
	v_pk_add_f32 v[28:29], v[4:5], v[4:5] op_sel:[0,1] op_sel_hi:[0,1]
	v_pk_add_f32 v[26:27], v[16:17], v[16:17] op_sel:[0,1] op_sel_hi:[0,1] neg_lo:[0,1] neg_hi:[0,1]
	s_mov_b64 s[42:43], 0x5003c0
	s_waitcnt vmcnt(3)
	v_mov_b32_e32 v9, v52
	v_mov_b32_e32 v52, v51
	v_mov_b32_e32 v8, v50
	v_pk_mul_f32 v[4:5], v[28:29], v[52:53]
	s_nop 0
	v_pk_fma_f32 v[4:5], v[26:27], v[8:9], v[4:5] neg_lo:[0,0,1] neg_hi:[0,0,1]
	s_nop 0
	v_pk_add_f32 v[56:57], v[2:3], v[4:5]
	s_waitcnt vmcnt(0)
	v_mov_b32_e32 v3, v70
	v_mov_b32_e32 v70, v69
	v_mov_b32_e32 v2, v68
	v_pk_mul_f32 v[4:5], v[28:29], v[70:71]
	s_nop 0
	v_pk_fma_f32 v[2:3], v[26:27], v[2:3], v[4:5] neg_lo:[0,0,1] neg_hi:[0,0,1]
	s_nop 0
	v_pk_add_f32 v[54:55], v[6:7], v[2:3]
	v_mov_b32_e32 v3, v64
	v_mov_b32_e32 v64, v63
	v_mov_b32_e32 v2, v62
	v_pk_mul_f32 v[4:5], v[28:29], v[64:65]
	s_nop 0
	v_pk_fma_f32 v[2:3], v[26:27], v[2:3], v[4:5] neg_lo:[0,0,1] neg_hi:[0,0,1]
	s_nop 0
	v_pk_add_f32 v[52:53], v[10:11], v[2:3]
	v_mov_b32_e32 v3, v60
	v_mov_b32_e32 v60, v59
	v_mov_b32_e32 v2, v58
	v_pk_mul_f32 v[4:5], v[28:29], v[60:61]
	s_nop 0
	v_pk_fma_f32 v[2:3], v[26:27], v[2:3], v[4:5] neg_lo:[0,0,1] neg_hi:[0,0,1]
	s_nop 0
	v_pk_add_f32 v[50:51], v[14:15], v[2:3]
	v_lshl_add_u64 v[14:15], v[48:49], 0, s[42:43]
	global_load_dwordx4 v[10:13], v[46:47], off offset:960
	global_load_dwordx4 v[2:5], v[14:15], off offset:48
	global_load_dwordx4 v[6:9], v[14:15], off offset:32
	s_nop 0
	global_load_dwordx4 v[14:17], v[14:15], off offset:16
	s_mov_b64 s[42:43], 0x400
	v_lshl_add_u64 v[38:39], v[38:39], 0, s[42:43]
	s_waitcnt vmcnt(3)
	v_mov_b32_e32 v47, v12
	v_mov_b32_e32 v12, v11
	v_mov_b32_e32 v46, v10
	v_pk_mul_f32 v[10:11], v[28:29], v[12:13]
	s_nop 0
	v_pk_fma_f32 v[10:11], v[26:27], v[46:47], v[10:11] neg_lo:[0,0,1] neg_hi:[0,0,1]
	s_nop 0
	v_pk_add_f32 v[58:59], v[24:25], v[10:11]
	s_waitcnt vmcnt(0)
	v_mov_b32_e32 v11, v16
	v_mov_b32_e32 v16, v15
	v_mov_b32_e32 v10, v14
	v_pk_mul_f32 v[12:13], v[28:29], v[16:17]
	s_nop 0
	v_pk_fma_f32 v[10:11], v[26:27], v[10:11], v[12:13] neg_lo:[0,0,1] neg_hi:[0,0,1]
	s_nop 0
	v_pk_add_f32 v[60:61], v[22:23], v[10:11]
	v_mov_b32_e32 v11, v8
	v_mov_b32_e32 v8, v7
	v_mov_b32_e32 v10, v6
	v_pk_mul_f32 v[6:7], v[28:29], v[8:9]
	s_nop 0
	v_pk_fma_f32 v[6:7], v[26:27], v[10:11], v[6:7] neg_lo:[0,0,1] neg_hi:[0,0,1]
	s_nop 0
	v_pk_add_f32 v[64:65], v[20:21], v[6:7]
	v_mov_b32_e32 v7, v4
	v_mov_b32_e32 v4, v3
	v_mov_b32_e32 v6, v2
	v_pk_mul_f32 v[2:3], v[28:29], v[4:5]
	s_nop 0
	v_pk_fma_f32 v[2:3], v[26:27], v[6:7], v[2:3] neg_lo:[0,0,1] neg_hi:[0,0,1]
	s_nop 0
	v_pk_add_f32 v[62:63], v[18:19], v[2:3]
	s_cbranch_scc0 .LBB0_324
	v_and_b32_e32 v2, 31, v66
	v_cmp_eq_u32_e32 vcc, 0, v2
	v_mov_b32_e32 v3, 0
	s_and_saveexec_b64 s[40:41], vcc
	s_cbranch_execz .LBB0_322
	v_lshl_or_b32 v4, v36, 4, v160
	v_readlane_b32 s0, v250, 33
	v_ashrrev_i32_e32 v5, 31, v4
	v_readlane_b32 s14, v250, 47
	v_readlane_b32 s15, v250, 48
	v_readlane_b32 s1, v250, 34
	v_readlane_b32 s2, v250, 35
	v_lshl_add_u64 v[4:5], v[4:5], 2, s[14:15]
	global_load_dword v3, v[4:5], off
	v_readlane_b32 s3, v250, 36
	v_readlane_b32 s4, v250, 37
	v_readlane_b32 s5, v250, 38
	v_readlane_b32 s6, v250, 39
	v_readlane_b32 s7, v250, 40
	v_readlane_b32 s8, v250, 41
	v_readlane_b32 s9, v250, 42
	v_readlane_b32 s10, v250, 43
	v_readlane_b32 s11, v250, 44
	v_readlane_b32 s12, v250, 45
	v_readlane_b32 s13, v250, 46
	s_branch .LBB0_322
